# v19
# speedup vs baseline: 1.1899x; 1.1899x over previous
.LBB1_20:
	s_and_b64 vcc, exec, s[0:1]
	s_cbranch_vccz .LBB1_31
	v_mov_b32_e32 v2, 0x18004
	v_readfirstlane_b32 s15, v0
	ds_read_b32 v215, v2
	s_lshr_b32 s23, s15, 6
	s_lshl_b32 s2, s23, 7
	s_mov_b32 s3, 0
	s_and_b32 s0, s15, 0xffffffc0
	s_lshl_b64 s[16:17], s[2:3], 2
	s_add_u32 s18, s26, s16
	s_addc_u32 s19, s27, s17
	v_mov_b32_e32 v211, 0
	s_waitcnt lgkmcnt(0)
	v_lshlrev_b32_e32 v216, 4, v215
	v_lshl_add_u64 v[118:119], s[18:19], 0, v[210:211]
	s_add_u32 s18, s38, s16
	v_or_b32_e32 v114, v216, v254
	s_addc_u32 s19, s39, s17
	s_add_u32 s16, s36, s16
	v_ashrrev_i32_e32 v115, 31, v114
	s_addc_u32 s17, s37, s17
	v_lshlrev_b64 v[2:3], 10, v[114:115]
	s_ashr_i32 s1, s0, 31
	v_lshl_add_u64 v[2:3], v[212:213], 0, v[2:3]
	s_lshl_b64 s[20:21], s[0:1], 2
	v_lshl_add_u64 v[14:15], v[2:3], 0, s[20:21]
	v_lshlrev_b64 v[16:17], 11, v[114:115]
	v_lshlrev_b32_e32 v18, 7, v215
	v_lshl_add_u64 v[122:123], s[18:19], 0, v[210:211]
	v_lshl_add_u64 v[120:121], s[16:17], 0, v[210:211]
	global_load_dwordx4 v[2:5], v[14:15], off offset:16
	global_load_dwordx4 v[6:9], v[14:15], off
	global_load_dwordx4 v[10:13], v[14:15], off offset:144
	global_load_dwordx4 v[24:27], v[14:15], off offset:128
	v_lshl_add_u64 v[14:15], v[118:119], 0, v[16:17]
	v_and_b32_e32 v210, 0x180, v18
	v_lshl_add_u64 v[18:19], v[14:15], 0, v[210:211]
	global_load_dwordx4 v[28:31], v[18:19], off
	global_load_dwordx4 v[32:35], v[18:19], off offset:16
	v_lshl_add_u64 v[18:19], v[120:121], 0, v[16:17]
	v_lshl_add_u64 v[20:21], v[18:19], 0, v[210:211]
	global_load_dwordx4 v[36:39], v[20:21], off
	global_load_dwordx4 v[40:43], v[20:21], off offset:16
	v_lshl_add_u64 v[22:23], v[122:123], 0, v[16:17]
	v_lshl_add_u64 v[16:17], v[22:23], 0, v[210:211]
	global_load_dwordx4 v[44:47], v[16:17], off
	global_load_dwordx4 v[48:51], v[16:17], off offset:16
	v_readfirstlane_b32 s30, v215
	s_add_i32 s26, s30, 1
	s_lshl_b32 s2, s26, 7
	s_and_b32 s2, s2, 0x180
	v_lshl_add_u64 v[16:17], v[14:15], 0, s[2:3]
	global_load_dwordx4 v[52:55], v[16:17], off
	global_load_dwordx4 v[56:59], v[16:17], off offset:16
	v_lshl_add_u64 v[16:17], v[18:19], 0, s[2:3]
	global_load_dwordx4 v[60:63], v[16:17], off
	global_load_dwordx4 v[64:67], v[16:17], off offset:16
	v_lshl_add_u64 v[16:17], v[22:23], 0, s[2:3]
	global_load_dwordx4 v[68:71], v[16:17], off offset:16
	global_load_dwordx4 v[72:75], v[16:17], off
	s_add_i32 s27, s30, 2
	s_lshl_b32 s16, s27, 7
	s_mov_b32 s19, s3
	s_and_b32 s18, s16, 0x180
	v_lshl_add_u64 v[20:21], v[14:15], 0, s[18:19]
	v_lshl_add_u64 v[16:17], v[18:19], 0, s[18:19]
	global_load_dwordx4 v[76:79], v[20:21], off offset:16
	global_load_dwordx4 v[90:93], v[20:21], off
	global_load_dwordx4 v[94:97], v[16:17], off offset:16
	global_load_dwordx4 v[98:101], v[16:17], off
	s_mov_b32 s14, 0xbfb8aa3b
	v_lshl_or_b32 v214, s23, 13, v1
	s_add_i32 s30, s30, 3
	s_lshl_b32 s16, s30, 7
	s_and_b32 s16, s16, 0x180
	s_mov_b32 s17, s3
	s_mov_b32 s22, 0x4038aa3b
	s_mov_b32 s31, 0x20000
	s_and_b32 s29, s29, 0xffff
	s_and_b32 s25, s25, 0xffff
	s_waitcnt vmcnt(19)
	v_pk_mul_f32 v[2:3], v[2:3], s[14:15] op_sel_hi:[1,0]
	s_waitcnt vmcnt(18)
	v_pk_mul_f32 v[6:7], v[6:7], s[14:15] op_sel_hi:[1,0]
	v_pk_mul_f32 v[8:9], v[8:9], s[14:15] op_sel_hi:[1,0]
	v_pk_mul_f32 v[4:5], v[4:5], s[14:15] op_sel_hi:[1,0]
	v_cvt_pk_f16_f32 v6, v6, v7
	s_waitcnt vmcnt(16)
	v_pk_mul_f32 v[16:17], v[24:25], s[14:15] op_sel_hi:[1,0]
	v_cvt_pk_f16_f32 v7, v8, v9
	v_cvt_pk_f16_f32 v8, v2, v3
	v_cvt_pk_f16_f32 v9, v4, v5
	v_accvgpr_write_b32 a0, v6
	v_pk_mul_f32 v[20:21], v[26:27], s[14:15] op_sel_hi:[1,0]
	v_pk_mul_f32 v[10:11], v[10:11], s[14:15] op_sel_hi:[1,0]
	v_pk_mul_f32 v[12:13], v[12:13], s[14:15] op_sel_hi:[1,0]
	v_accvgpr_write_b32 a1, v7
	v_accvgpr_write_b32 a2, v8
	v_accvgpr_write_b32 a3, v9
	v_cvt_pk_f16_f32 v6, v16, v17
	v_cvt_pk_f16_f32 v7, v20, v21
	v_cvt_pk_f16_f32 v8, v10, v11
	v_cvt_pk_f16_f32 v9, v12, v13
	v_accvgpr_write_b32 a4, v6
	ds_write_b128 v214, a[0:3] offset:32768
	ds_write_b128 v214, v[6:9] offset:33792
	v_accvgpr_write_b32 a5, v7
	v_accvgpr_write_b32 a6, v8
	v_accvgpr_write_b32 a7, v9
	s_waitcnt vmcnt(13)
	v_pk_mul_f32 v[6:7], v[36:37], s[14:15] op_sel_hi:[1,0]
	v_lshl_add_u64 v[8:9], v[22:23], 0, s[18:19]
	v_cvt_pk_f16_f32 v234, v6, v7
	v_pk_mul_f32 v[6:7], v[38:39], s[14:15] op_sel_hi:[1,0]
	v_pk_mul_f32 v[24:25], v[28:29], s[14:15] op_sel_hi:[1,0]
	v_cvt_pk_f16_f32 v235, v6, v7
	s_waitcnt vmcnt(12)
	v_pk_mul_f32 v[6:7], v[40:41], s[14:15] op_sel_hi:[1,0]
	v_pk_mul_f32 v[26:27], v[30:31], s[14:15] op_sel_hi:[1,0]
	v_cvt_pk_f16_f32 v236, v6, v7
	v_pk_mul_f32 v[6:7], v[42:43], s[14:15] op_sel_hi:[1,0]
	v_pk_mul_f32 v[28:29], v[32:33], s[14:15] op_sel_hi:[1,0]
	v_cvt_pk_f16_f32 v237, v6, v7
	s_waitcnt vmcnt(11)
	v_pk_mul_f32 v[6:7], v[44:45], s[14:15] op_sel_hi:[1,0]
	v_pk_mul_f32 v[30:31], v[34:35], s[14:15] op_sel_hi:[1,0]
	v_cvt_pk_f16_f32 v10, v6, v7
	v_pk_mul_f32 v[6:7], v[46:47], s[14:15] op_sel_hi:[1,0]
	global_load_dwordx4 v[32:35], v[8:9], off offset:16
	global_load_dwordx4 v[36:39], v[8:9], off
	v_cvt_pk_f16_f32 v11, v6, v7
	s_waitcnt vmcnt(12)
	v_pk_mul_f32 v[6:7], v[48:49], s[14:15] op_sel_hi:[1,0]
	v_lshl_add_u64 v[8:9], v[22:23], 0, s[16:17]
	v_cvt_pk_f16_f32 v12, v6, v7
	v_lshl_add_u64 v[6:7], v[14:15], 0, s[16:17]
	global_load_dwordx4 v[40:43], v[6:7], off offset:16
	global_load_dwordx4 v[44:47], v[6:7], off
	v_pk_mul_f32 v[6:7], v[50:51], s[14:15] op_sel_hi:[1,0]
	v_cvt_pk_f16_f32 v2, v24, v25
	v_cvt_pk_f16_f32 v13, v6, v7
	s_waitcnt vmcnt(13)
	v_pk_mul_f32 v[6:7], v[52:53], s[14:15] op_sel_hi:[1,0]
	v_cvt_pk_f16_f32 v4, v28, v29
	v_cvt_pk_f16_f32 v14, v6, v7
	v_pk_mul_f32 v[6:7], v[54:55], s[14:15] op_sel_hi:[1,0]
	v_cvt_pk_f16_f32 v3, v26, v27
	v_cvt_pk_f16_f32 v15, v6, v7
	s_waitcnt vmcnt(12)
	v_pk_mul_f32 v[6:7], v[56:57], s[14:15] op_sel_hi:[1,0]
	v_cvt_pk_f16_f32 v5, v30, v31
	v_cvt_pk_f16_f32 v16, v6, v7
	v_lshl_add_u64 v[6:7], v[18:19], 0, s[16:17]
	global_load_dwordx4 v[48:51], v[6:7], off offset:16
	global_load_dwordx4 v[52:55], v[6:7], off
	v_pk_mul_f32 v[6:7], v[58:59], s[14:15] op_sel_hi:[1,0]
	s_waitcnt vmcnt(5)
	v_pk_mul_f32 v[32:33], v[32:33], s[14:15] op_sel_hi:[1,0]
	v_cvt_pk_f16_f32 v17, v6, v7
	v_pk_mul_f32 v[6:7], v[60:61], s[14:15] op_sel_hi:[1,0]
	v_cvt_pk_f16_f32 v32, v32, v33
	v_cvt_pk_f16_f32 v18, v6, v7
	v_pk_mul_f32 v[6:7], v[62:63], s[14:15] op_sel_hi:[1,0]
	s_nop 0
	v_cvt_pk_f16_f32 v19, v6, v7
	v_pk_mul_f32 v[6:7], v[64:65], s[14:15] op_sel_hi:[1,0]
	s_nop 0
	v_cvt_pk_f16_f32 v20, v6, v7
	v_pk_mul_f32 v[6:7], v[66:67], s[14:15] op_sel_hi:[1,0]
	global_load_dwordx4 v[64:67], v[8:9], off offset:16
	global_load_dwordx4 v[102:105], v[8:9], off
	v_add_u32_e32 v8, 0x200, v114
	v_ashrrev_i32_e32 v9, 31, v8
	v_cvt_pk_f16_f32 v21, v6, v7
	v_pk_mul_f32 v[6:7], v[72:73], s[14:15] op_sel_hi:[1,0]
	v_lshlrev_b64 v[24:25], 10, v[8:9]
	v_cvt_pk_f16_f32 v22, v6, v7
	v_pk_mul_f32 v[6:7], v[74:75], s[14:15] op_sel_hi:[1,0]
	v_lshl_add_u64 v[24:25], v[212:213], 0, v[24:25]
	v_lshl_add_u64 v[28:29], v[24:25], 0, s[20:21]
	v_cvt_pk_f16_f32 v23, v6, v7
	v_pk_mul_f32 v[6:7], v[68:69], s[14:15] op_sel_hi:[1,0]
	global_load_dwordx4 v[72:75], v[28:29], off offset:16
	global_load_dwordx4 v[106:109], v[28:29], off
	v_cvt_pk_f16_f32 v24, v6, v7
	v_pk_mul_f32 v[6:7], v[70:71], s[14:15] op_sel_hi:[1,0]
	s_nop 0
	v_cvt_pk_f16_f32 v25, v6, v7
	v_pk_mul_f32 v[6:7], v[90:91], s[14:15] op_sel_hi:[1,0]
	s_nop 0
	v_cvt_pk_f16_f32 v26, v6, v7
	v_pk_mul_f32 v[6:7], v[92:93], s[14:15] op_sel_hi:[1,0]
	global_load_dwordx4 v[68:71], v[28:29], off offset:144
	global_load_dwordx4 v[90:93], v[28:29], off offset:128
	v_cvt_pk_f16_f32 v27, v6, v7
	v_pk_mul_f32 v[6:7], v[76:77], s[14:15] op_sel_hi:[1,0]
	s_nop 0
	v_cvt_pk_f16_f32 v28, v6, v7
	v_pk_mul_f32 v[6:7], v[78:79], s[14:15] op_sel_hi:[1,0]
	s_nop 0
	v_cvt_pk_f16_f32 v29, v6, v7
	v_pk_mul_f32 v[6:7], v[98:99], s[14:15] op_sel_hi:[1,0]
	s_nop 0
	v_cvt_pk_f16_f32 v60, v6, v7
	v_pk_mul_f32 v[6:7], v[100:101], s[14:15] op_sel_hi:[1,0]
	s_nop 0
	v_cvt_pk_f16_f32 v61, v6, v7
	v_lshlrev_b64 v[6:7], 11, v[8:9]
	v_lshl_add_u64 v[8:9], v[118:119], 0, v[6:7]
	v_lshl_add_u64 v[30:31], v[8:9], 0, v[210:211]
	global_load_dwordx4 v[76:79], v[30:31], off offset:16
	global_load_dwordx4 v[98:101], v[30:31], off
	v_pk_mul_f32 v[30:31], v[94:95], s[14:15] op_sel_hi:[1,0]
	v_lshl_add_u64 v[58:59], v[120:121], 0, v[6:7]
	v_cvt_pk_f16_f32 v62, v30, v31
	v_pk_mul_f32 v[30:31], v[96:97], s[14:15] op_sel_hi:[1,0]
	s_nop 0
	v_cvt_pk_f16_f32 v63, v30, v31
	v_lshl_add_u64 v[30:31], v[58:59], 0, v[210:211]
	global_load_dwordx4 v[94:97], v[30:31], off offset:16
	global_load_dwordx4 v[110:113], v[30:31], off
	ds_write_b128 v214, v[60:63]
	v_lshl_add_u64 v[62:63], v[122:123], 0, v[6:7]
	v_lshl_add_u64 v[6:7], v[62:63], 0, v[210:211]
	global_load_dwordx4 v[134:137], v[6:7], off offset:16
	global_load_dwordx4 v[138:141], v[6:7], off
	v_pk_mul_f32 v[6:7], v[34:35], s[14:15] op_sel_hi:[1,0]
	s_waitcnt vmcnt(16)
	v_pk_mul_f32 v[30:31], v[36:37], s[14:15] op_sel_hi:[1,0]
	v_cvt_pk_f16_f32 v33, v6, v7
	s_waitcnt vmcnt(14)
	v_pk_mul_f32 v[6:7], v[44:45], s[14:15] op_sel_hi:[1,0]
	v_pk_mul_f32 v[36:37], v[38:39], s[14:15] op_sel_hi:[1,0]
	v_cvt_pk_f16_f32 v34, v6, v7
	v_pk_mul_f32 v[6:7], v[46:47], s[14:15] op_sel_hi:[1,0]
	v_cvt_pk_f16_f32 v30, v30, v31
	v_cvt_pk_f16_f32 v35, v6, v7
	v_pk_mul_f32 v[6:7], v[40:41], s[14:15] op_sel_hi:[1,0]
	v_cvt_pk_f16_f32 v31, v36, v37
	v_cvt_pk_f16_f32 v36, v6, v7
	v_lshl_add_u64 v[6:7], v[8:9], 0, s[2:3]
	global_load_dwordx4 v[142:145], v[6:7], off offset:16
	global_load_dwordx4 v[146:149], v[6:7], off
	v_pk_mul_f32 v[6:7], v[42:43], s[14:15] op_sel_hi:[1,0]
	v_lshl_add_u64 v[42:43], v[58:59], 0, s[18:19]
	v_cvt_pk_f16_f32 v37, v6, v7
	s_waitcnt vmcnt(14)
	v_pk_mul_f32 v[6:7], v[52:53], s[14:15] op_sel_hi:[1,0]
	v_lshl_add_u64 v[46:47], v[62:63], 0, s[18:19]
	v_cvt_pk_f16_f32 v38, v6, v7
	v_pk_mul_f32 v[6:7], v[54:55], s[14:15] op_sel_hi:[1,0]
	s_nop 0
	v_cvt_pk_f16_f32 v39, v6, v7
	v_pk_mul_f32 v[6:7], v[48:49], s[14:15] op_sel_hi:[1,0]
	s_nop 0
	v_cvt_pk_f16_f32 v40, v6, v7
	v_lshl_add_u64 v[6:7], v[58:59], 0, s[2:3]
	global_load_dwordx4 v[150:153], v[6:7], off offset:16
	global_load_dwordx4 v[154:157], v[6:7], off
	v_pk_mul_f32 v[6:7], v[50:51], s[14:15] op_sel_hi:[1,0]
	s_nop 0
	v_cvt_pk_f16_f32 v41, v6, v7
	ds_write_b128 v214, v[38:41] offset:1024
	s_waitcnt vmcnt(14)
	v_pk_mul_f32 v[6:7], v[102:103], s[14:15] op_sel_hi:[1,0]
	v_lshl_add_u64 v[40:41], v[62:63], 0, s[2:3]
	v_cvt_pk_f16_f32 v38, v6, v7
	v_pk_mul_f32 v[6:7], v[104:105], s[14:15] op_sel_hi:[1,0]
	global_load_dwordx4 v[102:105], v[40:41], off offset:16
	global_load_dwordx4 v[158:161], v[40:41], off
	v_cvt_pk_f16_f32 v39, v6, v7
	v_pk_mul_f32 v[6:7], v[64:65], s[14:15] op_sel_hi:[1,0]
	s_waitcnt vmcnt(1)
	v_pk_mul_f32 v[64:65], v[102:103], s[14:15] op_sel_hi:[1,0]
	v_cvt_pk_f16_f32 v40, v6, v7
	v_pk_mul_f32 v[6:7], v[66:67], s[14:15] op_sel_hi:[1,0]
	v_pk_mul_f32 v[66:67], v[104:105], s[14:15] op_sel_hi:[1,0]
	v_cvt_pk_f16_f32 v41, v6, v7
	v_pk_mul_f32 v[6:7], v[106:107], s[14:15] op_sel_hi:[1,0]
	v_cvt_pk_f16_f32 v64, v64, v65
	v_cvt_pk_f16_f32 v126, v6, v7
	v_pk_mul_f32 v[6:7], v[108:109], s[14:15] op_sel_hi:[1,0]
	v_cvt_pk_f16_f32 v65, v66, v67
	v_cvt_pk_f16_f32 v127, v6, v7
	v_pk_mul_f32 v[6:7], v[72:73], s[14:15] op_sel_hi:[1,0]
	s_nop 0
	v_cvt_pk_f16_f32 v128, v6, v7
	v_pk_mul_f32 v[6:7], v[74:75], s[14:15] op_sel_hi:[1,0]
	s_nop 0
	v_cvt_pk_f16_f32 v129, v6, v7
	ds_write_b128 v214, v[126:129] offset:34816
	v_lshl_add_u64 v[6:7], v[8:9], 0, s[18:19]
	global_load_dwordx4 v[72:75], v[6:7], off offset:16
	global_load_dwordx4 v[106:109], v[6:7], off
	v_pk_mul_f32 v[6:7], v[90:91], s[14:15] op_sel_hi:[1,0]
	s_waitcnt vmcnt(0)
	v_pk_mul_f32 v[66:67], v[106:107], s[14:15] op_sel_hi:[1,0]
	v_cvt_pk_f16_f32 v130, v6, v7
	v_pk_mul_f32 v[6:7], v[92:93], s[14:15] op_sel_hi:[1,0]
	global_load_dwordx4 v[90:93], v[42:43], off offset:16
	global_load_dwordx4 v[162:165], v[42:43], off
	v_cvt_pk_f16_f32 v131, v6, v7
	v_pk_mul_f32 v[6:7], v[68:69], s[14:15] op_sel_hi:[1,0]
	v_pk_mul_f32 v[68:69], v[108:109], s[14:15] op_sel_hi:[1,0]
	v_cvt_pk_f16_f32 v132, v6, v7
	v_pk_mul_f32 v[6:7], v[70:71], s[14:15] op_sel_hi:[1,0]
	v_cvt_pk_f16_f32 v66, v66, v67
	v_cvt_pk_f16_f32 v133, v6, v7
	v_pk_mul_f32 v[6:7], v[98:99], s[14:15] op_sel_hi:[1,0]
	ds_write_b128 v214, v[130:133] offset:35840
	v_cvt_pk_f16_f32 v42, v6, v7
	v_pk_mul_f32 v[6:7], v[100:101], s[14:15] op_sel_hi:[1,0]
	v_cvt_pk_f16_f32 v67, v68, v69
	v_cvt_pk_f16_f32 v43, v6, v7
	v_pk_mul_f32 v[6:7], v[76:77], s[14:15] op_sel_hi:[1,0]
	v_pk_mul_f32 v[68:69], v[72:73], s[14:15] op_sel_hi:[1,0]
	v_cvt_pk_f16_f32 v44, v6, v7
	v_pk_mul_f32 v[6:7], v[78:79], s[14:15] op_sel_hi:[1,0]
	global_load_dwordx4 v[76:79], v[46:47], off offset:16
	global_load_dwordx4 v[98:101], v[46:47], off
	v_cvt_pk_f16_f32 v45, v6, v7
	v_pk_mul_f32 v[6:7], v[110:111], s[14:15] op_sel_hi:[1,0]
	v_cvt_pk_f16_f32 v68, v68, v69
	v_cvt_pk_f16_f32 v46, v6, v7
	v_pk_mul_f32 v[6:7], v[112:113], s[14:15] op_sel_hi:[1,0]
	s_nop 0
	v_cvt_pk_f16_f32 v47, v6, v7
	v_pk_mul_f32 v[6:7], v[94:95], s[14:15] op_sel_hi:[1,0]
	s_nop 0
	v_cvt_pk_f16_f32 v48, v6, v7
	v_pk_mul_f32 v[6:7], v[96:97], s[14:15] op_sel_hi:[1,0]
	s_nop 0
	v_cvt_pk_f16_f32 v49, v6, v7
	v_pk_mul_f32 v[6:7], v[138:139], s[14:15] op_sel_hi:[1,0]
	s_nop 0
	v_cvt_pk_f16_f32 v50, v6, v7
	v_pk_mul_f32 v[6:7], v[140:141], s[14:15] op_sel_hi:[1,0]
	s_nop 0
	v_cvt_pk_f16_f32 v51, v6, v7
	v_pk_mul_f32 v[6:7], v[134:135], s[14:15] op_sel_hi:[1,0]
	s_nop 0
	v_cvt_pk_f16_f32 v52, v6, v7
	v_lshl_add_u64 v[6:7], v[8:9], 0, s[16:17]
	global_load_dwordx4 v[94:97], v[6:7], off offset:16
	global_load_dwordx4 v[138:141], v[6:7], off
	v_pk_mul_f32 v[6:7], v[136:137], s[14:15] op_sel_hi:[1,0]
	v_lshl_add_u64 v[8:9], v[62:63], 0, s[16:17]
	v_cvt_pk_f16_f32 v53, v6, v7
	v_pk_mul_f32 v[6:7], v[146:147], s[14:15] op_sel_hi:[1,0]
	s_nop 0
	v_cvt_pk_f16_f32 v54, v6, v7
	v_pk_mul_f32 v[6:7], v[148:149], s[14:15] op_sel_hi:[1,0]
	s_nop 0
	v_cvt_pk_f16_f32 v55, v6, v7
	v_pk_mul_f32 v[6:7], v[142:143], s[14:15] op_sel_hi:[1,0]
	s_nop 0
	v_cvt_pk_f16_f32 v56, v6, v7
	v_lshl_add_u64 v[6:7], v[58:59], 0, s[16:17]
	global_load_dwordx4 v[134:137], v[6:7], off offset:16
	global_load_dwordx4 v[146:149], v[6:7], off
	v_pk_mul_f32 v[6:7], v[144:145], s[14:15] op_sel_hi:[1,0]
	s_nop 0
	v_cvt_pk_f16_f32 v57, v6, v7
	v_pk_mul_f32 v[6:7], v[154:155], s[14:15] op_sel_hi:[1,0]
	s_nop 0
	v_cvt_pk_f16_f32 v58, v6, v7
	v_pk_mul_f32 v[6:7], v[156:157], s[14:15] op_sel_hi:[1,0]
	s_nop 0
	v_cvt_pk_f16_f32 v59, v6, v7
	v_pk_mul_f32 v[6:7], v[150:151], s[14:15] op_sel_hi:[1,0]
	s_nop 0
	v_cvt_pk_f16_f32 v60, v6, v7
	v_pk_mul_f32 v[6:7], v[152:153], s[14:15] op_sel_hi:[1,0]
	global_load_dwordx4 v[142:145], v[8:9], off offset:16
	global_load_dwordx4 v[150:153], v[8:9], off
	v_cvt_pk_f16_f32 v61, v6, v7
	v_pk_mul_f32 v[6:7], v[158:159], s[14:15] op_sel_hi:[1,0]
	s_nop 0
	v_cvt_pk_f16_f32 v62, v6, v7
	v_pk_mul_f32 v[6:7], v[160:161], s[14:15] op_sel_hi:[1,0]
	s_nop 0
	v_cvt_pk_f16_f32 v63, v6, v7
	v_add_u32_e32 v6, 0x400, v114
	v_ashrrev_i32_e32 v7, 31, v6
	v_lshlrev_b64 v[8:9], 10, v[6:7]
	v_lshl_add_u64 v[8:9], v[212:213], 0, v[8:9]
	v_lshl_add_u64 v[8:9], v[8:9], 0, s[20:21]
	global_load_dwordx4 v[154:157], v[8:9], off offset:16
	global_load_dwordx4 v[158:161], v[8:9], off
	global_load_dwordx4 v[102:105], v[8:9], off offset:144
	global_load_dwordx4 v[108:111], v[8:9], off offset:128
	v_lshlrev_b64 v[6:7], 11, v[6:7]
	v_pk_mul_f32 v[8:9], v[74:75], s[14:15] op_sel_hi:[1,0]
	v_lshl_add_u64 v[82:83], v[118:119], 0, v[6:7]
	v_cvt_pk_f16_f32 v69, v8, v9
	s_waitcnt vmcnt(12)
	v_pk_mul_f32 v[8:9], v[162:163], s[14:15] op_sel_hi:[1,0]
	v_lshl_add_u64 v[72:73], v[82:83], 0, v[210:211]
	v_cvt_pk_f16_f32 v70, v8, v9
	v_pk_mul_f32 v[8:9], v[164:165], s[14:15] op_sel_hi:[1,0]
	global_load_dwordx4 v[162:165], v[72:73], off offset:16
	global_load_dwordx4 v[166:169], v[72:73], off
	v_cvt_pk_f16_f32 v71, v8, v9
	v_pk_mul_f32 v[8:9], v[90:91], s[14:15] op_sel_hi:[1,0]
	v_lshl_add_u64 v[106:107], v[120:121], 0, v[6:7]
	v_cvt_pk_f16_f32 v72, v8, v9
	v_pk_mul_f32 v[8:9], v[92:93], s[14:15] op_sel_hi:[1,0]
	v_lshl_add_u64 v[112:113], v[122:123], 0, v[6:7]
	v_cvt_pk_f16_f32 v73, v8, v9
	ds_write_b128 v214, v[70:73] offset:2048
	s_waitcnt vmcnt(12)
	v_pk_mul_f32 v[8:9], v[98:99], s[14:15] op_sel_hi:[1,0]
	v_lshl_add_u64 v[72:73], v[106:107], 0, v[210:211]
	v_cvt_pk_f16_f32 v70, v8, v9
	v_pk_mul_f32 v[8:9], v[100:101], s[14:15] op_sel_hi:[1,0]
	global_load_dwordx4 v[98:101], v[72:73], off offset:16
	global_load_dwordx4 v[170:173], v[72:73], off
	v_lshl_add_u64 v[6:7], v[112:113], 0, v[210:211]
	global_load_dwordx4 v[186:189], v[6:7], off offset:16
	global_load_dwordx4 v[190:193], v[6:7], off
	v_cvt_pk_f16_f32 v71, v8, v9
	v_pk_mul_f32 v[8:9], v[76:77], s[14:15] op_sel_hi:[1,0]
	s_waitcnt vmcnt(14)
	v_pk_mul_f32 v[6:7], v[138:139], s[14:15] op_sel_hi:[1,0]
	v_cvt_pk_f16_f32 v72, v8, v9
	v_pk_mul_f32 v[8:9], v[78:79], s[14:15] op_sel_hi:[1,0]
	v_cvt_pk_f16_f32 v74, v6, v7
	v_cvt_pk_f16_f32 v73, v8, v9
	v_pk_mul_f32 v[6:7], v[140:141], s[14:15] op_sel_hi:[1,0]
	v_lshl_add_u64 v[8:9], v[82:83], 0, s[2:3]
	v_cvt_pk_f16_f32 v75, v6, v7
	v_pk_mul_f32 v[6:7], v[94:95], s[14:15] op_sel_hi:[1,0]
	global_load_dwordx4 v[138:141], v[8:9], off offset:16
	global_load_dwordx4 v[194:197], v[8:9], off
	v_cvt_pk_f16_f32 v76, v6, v7
	v_pk_mul_f32 v[6:7], v[96:97], s[14:15] op_sel_hi:[1,0]
	v_lshl_add_u64 v[8:9], v[106:107], 0, s[2:3]
	v_cvt_pk_f16_f32 v77, v6, v7
	s_waitcnt vmcnt(14)
	v_pk_mul_f32 v[6:7], v[146:147], s[14:15] op_sel_hi:[1,0]
	s_nop 0
	v_cvt_pk_f16_f32 v78, v6, v7
	v_pk_mul_f32 v[6:7], v[148:149], s[14:15] op_sel_hi:[1,0]
	s_nop 0
	v_cvt_pk_f16_f32 v79, v6, v7
	v_pk_mul_f32 v[6:7], v[134:135], s[14:15] op_sel_hi:[1,0]
	s_nop 0
	v_cvt_pk_f16_f32 v80, v6, v7
	v_pk_mul_f32 v[6:7], v[136:137], s[14:15] op_sel_hi:[1,0]
	global_load_dwordx4 v[134:137], v[8:9], off offset:16
	global_load_dwordx4 v[146:149], v[8:9], off
	v_cvt_pk_f16_f32 v81, v6, v7
	ds_write_b128 v214, v[78:81] offset:3072
	v_lshl_add_u64 v[8:9], v[112:113], 0, s[2:3]
	s_waitcnt vmcnt(14)
	v_pk_mul_f32 v[6:7], v[150:151], s[14:15] op_sel_hi:[1,0]
	s_nop 0
	v_cvt_pk_f16_f32 v78, v6, v7
	v_pk_mul_f32 v[6:7], v[152:153], s[14:15] op_sel_hi:[1,0]
	global_load_dwordx4 v[150:153], v[8:9], off offset:16
	global_load_dwordx4 v[198:201], v[8:9], off
	v_cvt_pk_f16_f32 v79, v6, v7
	v_pk_mul_f32 v[6:7], v[142:143], s[14:15] op_sel_hi:[1,0]
	v_lshl_add_u64 v[8:9], v[106:107], 0, s[18:19]
	v_cvt_pk_f16_f32 v80, v6, v7
	v_pk_mul_f32 v[6:7], v[144:145], s[14:15] op_sel_hi:[1,0]
	s_nop 0
	v_cvt_pk_f16_f32 v81, v6, v7
	s_waitcnt vmcnt(14)
	v_pk_mul_f32 v[6:7], v[158:159], s[22:23] op_sel_hi:[1,0]
	s_nop 0
	v_cvt_pk_f16_f32 v174, v6, v7
	v_pk_mul_f32 v[6:7], v[160:161], s[22:23] op_sel_hi:[1,0]
	s_nop 0
	v_cvt_pk_f16_f32 v175, v6, v7
	v_pk_mul_f32 v[6:7], v[154:155], s[22:23] op_sel_hi:[1,0]
	s_nop 0
	v_cvt_pk_f16_f32 v176, v6, v7
	v_pk_mul_f32 v[6:7], v[156:157], s[22:23] op_sel_hi:[1,0]
	s_nop 0
	v_cvt_pk_f16_f32 v177, v6, v7
	ds_write_b128 v214, v[174:177] offset:36864
	v_lshl_add_u64 v[6:7], v[82:83], 0, s[18:19]
	global_load_dwordx4 v[142:145], v[6:7], off offset:16
	global_load_dwordx4 v[154:157], v[6:7], off
	s_waitcnt vmcnt(14)
	v_pk_mul_f32 v[6:7], v[108:109], s[22:23] op_sel_hi:[1,0]
	global_load_dwordx4 v[158:161], v[8:9], off offset:16
	global_load_dwordx4 v[202:205], v[8:9], off
	v_cvt_pk_f16_f32 v182, v6, v7
	v_pk_mul_f32 v[6:7], v[110:111], s[22:23] op_sel_hi:[1,0]
	s_nop 0
	v_cvt_pk_f16_f32 v183, v6, v7
	v_pk_mul_f32 v[6:7], v[102:103], s[22:23] op_sel_hi:[1,0]
	s_nop 0
	v_cvt_pk_f16_f32 v184, v6, v7
	v_pk_mul_f32 v[6:7], v[104:105], s[22:23] op_sel_hi:[1,0]
	s_nop 0
	v_cvt_pk_f16_f32 v185, v6, v7
	s_waitcnt vmcnt(14)
	v_pk_mul_f32 v[6:7], v[166:167], s[22:23] op_sel_hi:[1,0]
	ds_write_b128 v214, v[182:185] offset:37888
	v_cvt_pk_f16_f32 v90, v6, v7
	v_pk_mul_f32 v[6:7], v[168:169], s[22:23] op_sel_hi:[1,0]
	s_nop 0
	v_cvt_pk_f16_f32 v91, v6, v7
	v_lshl_add_u64 v[6:7], v[112:113], 0, s[18:19]
	global_load_dwordx4 v[206:209], v[6:7], off offset:16
	global_load_dwordx4 v[166:169], v[6:7], off
	v_pk_mul_f32 v[6:7], v[162:163], s[22:23] op_sel_hi:[1,0]
	s_nop 0
	v_cvt_pk_f16_f32 v92, v6, v7
	v_pk_mul_f32 v[6:7], v[164:165], s[22:23] op_sel_hi:[1,0]
	s_nop 0
	v_cvt_pk_f16_f32 v93, v6, v7
	s_waitcnt vmcnt(14)
	v_pk_mul_f32 v[6:7], v[170:171], s[22:23] op_sel_hi:[1,0]
	s_nop 0
	v_cvt_pk_f16_f32 v94, v6, v7
	v_pk_mul_f32 v[6:7], v[172:173], s[22:23] op_sel_hi:[1,0]
	s_nop 0
	v_cvt_pk_f16_f32 v95, v6, v7
	v_pk_mul_f32 v[6:7], v[98:99], s[22:23] op_sel_hi:[1,0]
	s_nop 0
	v_cvt_pk_f16_f32 v96, v6, v7
	v_pk_mul_f32 v[6:7], v[100:101], s[22:23] op_sel_hi:[1,0]
	s_nop 0
	v_cvt_pk_f16_f32 v97, v6, v7
	s_waitcnt vmcnt(12)
	v_pk_mul_f32 v[6:7], v[190:191], s[22:23] op_sel_hi:[1,0]
	s_nop 0
	v_cvt_pk_f16_f32 v98, v6, v7
	v_lshl_add_u64 v[6:7], v[82:83], 0, s[16:17]
	global_load_dwordx4 v[162:165], v[6:7], off offset:16
	global_load_dwordx4 v[170:173], v[6:7], off
	v_pk_mul_f32 v[6:7], v[192:193], s[22:23] op_sel_hi:[1,0]
	s_waitcnt vmcnt(9)
	v_pk_mul_f32 v[82:83], v[152:153], s[22:23] op_sel_hi:[1,0]
	v_cvt_pk_f16_f32 v99, v6, v7
	v_pk_mul_f32 v[6:7], v[186:187], s[22:23] op_sel_hi:[1,0]
	s_nop 0
	v_cvt_pk_f16_f32 v100, v6, v7
	v_pk_mul_f32 v[6:7], v[188:189], s[22:23] op_sel_hi:[1,0]
	s_nop 0
	v_cvt_pk_f16_f32 v101, v6, v7
	v_pk_mul_f32 v[6:7], v[194:195], s[22:23] op_sel_hi:[1,0]
	s_nop 0
	v_cvt_pk_f16_f32 v102, v6, v7
	v_pk_mul_f32 v[6:7], v[196:197], s[22:23] op_sel_hi:[1,0]
	s_nop 0
	v_cvt_pk_f16_f32 v103, v6, v7
	v_pk_mul_f32 v[6:7], v[138:139], s[22:23] op_sel_hi:[1,0]
	s_nop 0
	v_cvt_pk_f16_f32 v104, v6, v7
	v_lshl_add_u64 v[6:7], v[106:107], 0, s[16:17]
	global_load_dwordx4 v[186:189], v[6:7], off offset:16
	global_load_dwordx4 v[190:193], v[6:7], off
	v_pk_mul_f32 v[6:7], v[140:141], s[22:23] op_sel_hi:[1,0]
	s_nop 0
	v_cvt_pk_f16_f32 v105, v6, v7
	v_pk_mul_f32 v[6:7], v[146:147], s[22:23] op_sel_hi:[1,0]
	s_nop 0
	v_cvt_pk_f16_f32 v106, v6, v7
	v_pk_mul_f32 v[6:7], v[148:149], s[22:23] op_sel_hi:[1,0]
	s_nop 0
	v_cvt_pk_f16_f32 v107, v6, v7
	v_pk_mul_f32 v[6:7], v[134:135], s[22:23] op_sel_hi:[1,0]
	s_nop 0
	v_cvt_pk_f16_f32 v108, v6, v7
	v_pk_mul_f32 v[6:7], v[136:137], s[22:23] op_sel_hi:[1,0]
	s_nop 0
	v_cvt_pk_f16_f32 v109, v6, v7
	s_waitcnt vmcnt(10)
	v_pk_mul_f32 v[6:7], v[198:199], s[22:23] op_sel_hi:[1,0]
	s_nop 0
	v_cvt_pk_f16_f32 v110, v6, v7
	v_lshl_add_u64 v[6:7], v[112:113], 0, s[16:17]
	global_load_dwordx4 v[136:139], v[6:7], off offset:16
	global_load_dwordx4 v[146:149], v[6:7], off
	v_pk_mul_f32 v[6:7], v[200:201], s[22:23] op_sel_hi:[1,0]
	v_cvt_pk_f16_f32 v113, v82, v83
	v_cvt_pk_f16_f32 v111, v6, v7
	v_pk_mul_f32 v[6:7], v[150:151], s[22:23] op_sel_hi:[1,0]
	s_waitcnt vmcnt(10)
	v_pk_mul_f32 v[82:83], v[154:155], s[22:23] op_sel_hi:[1,0]
	v_cvt_pk_f16_f32 v112, v6, v7
	v_add_u32_e32 v6, 0x600, v114
	v_ashrrev_i32_e32 v7, 31, v6
	v_lshlrev_b64 v[8:9], 10, v[6:7]
	v_lshl_add_u64 v[8:9], v[212:213], 0, v[8:9]
	v_lshl_add_u64 v[8:9], v[8:9], 0, s[20:21]
	global_load_dwordx4 v[194:197], v[8:9], off offset:16
	global_load_dwordx4 v[198:201], v[8:9], off
	v_cvt_pk_f16_f32 v114, v82, v83
	v_pk_mul_f32 v[82:83], v[156:157], s[22:23] op_sel_hi:[1,0]
	v_lshlrev_b64 v[6:7], 11, v[6:7]
	v_cvt_pk_f16_f32 v115, v82, v83
	v_pk_mul_f32 v[82:83], v[142:143], s[22:23] op_sel_hi:[1,0]
	global_load_dwordx4 v[140:143], v[8:9], off offset:144
	global_load_dwordx4 v[150:153], v[8:9], off offset:128
	s_waitcnt vmcnt(12)
	v_pk_mul_f32 v[8:9], v[202:203], s[22:23] op_sel_hi:[1,0]
	v_cvt_pk_f16_f32 v116, v82, v83
	v_cvt_pk_f16_f32 v154, v8, v9
	v_pk_mul_f32 v[8:9], v[204:205], s[22:23] op_sel_hi:[1,0]
	v_pk_mul_f32 v[82:83], v[144:145], s[22:23] op_sel_hi:[1,0]
	v_cvt_pk_f16_f32 v155, v8, v9
	v_pk_mul_f32 v[8:9], v[158:159], s[22:23] op_sel_hi:[1,0]
	v_lshl_add_u64 v[144:145], v[118:119], 0, v[6:7]
	v_cvt_pk_f16_f32 v156, v8, v9
	v_pk_mul_f32 v[8:9], v[160:161], s[22:23] op_sel_hi:[1,0]
	v_cvt_pk_f16_f32 v117, v82, v83
	v_cvt_pk_f16_f32 v157, v8, v9
	s_waitcnt vmcnt(10)
	v_pk_mul_f32 v[8:9], v[166:167], s[22:23] op_sel_hi:[1,0]
	ds_write_b128 v214, v[154:157] offset:4096
	v_lshl_add_u64 v[82:83], v[144:145], 0, v[210:211]
	v_cvt_pk_f16_f32 v118, v8, v9
	v_pk_mul_f32 v[8:9], v[168:169], s[22:23] op_sel_hi:[1,0]
	v_lshl_add_u64 v[168:169], v[120:121], 0, v[6:7]
	v_lshl_add_u64 v[166:167], v[122:123], 0, v[6:7]
	global_load_dwordx4 v[154:157], v[82:83], off offset:16
	global_load_dwordx4 v[158:161], v[82:83], off
	v_cvt_pk_f16_f32 v119, v8, v9
	v_pk_mul_f32 v[8:9], v[206:207], s[22:23] op_sel_hi:[1,0]
	v_lshl_add_u64 v[82:83], v[168:169], 0, v[210:211]
	v_lshl_add_u64 v[6:7], v[166:167], 0, v[210:211]
	global_load_dwordx4 v[222:225], v[82:83], off offset:16
	global_load_dwordx4 v[226:229], v[82:83], off
	v_cvt_pk_f16_f32 v120, v8, v9
	v_pk_mul_f32 v[8:9], v[208:209], s[22:23] op_sel_hi:[1,0]
	global_load_dwordx4 v[206:209], v[6:7], off offset:16
	global_load_dwordx4 v[86:89], v[6:7], off
	s_waitcnt vmcnt(14)
	v_pk_mul_f32 v[6:7], v[172:173], s[22:23] op_sel_hi:[1,0]
	v_cvt_pk_f16_f32 v121, v8, v9
	v_cvt_pk_f16_f32 v123, v6, v7
	v_pk_mul_f32 v[6:7], v[162:163], s[22:23] op_sel_hi:[1,0]
	v_pk_mul_f32 v[8:9], v[170:171], s[22:23] op_sel_hi:[1,0]
	v_cvt_pk_f16_f32 v124, v6, v7
	v_lshl_add_u64 v[6:7], v[144:145], 0, s[2:3]
	global_load_dwordx4 v[170:173], v[6:7], off offset:16
	global_load_dwordx4 v[82:85], v[6:7], off
	v_pk_mul_f32 v[6:7], v[164:165], s[22:23] op_sel_hi:[1,0]
	v_cvt_pk_f16_f32 v122, v8, v9
	v_cvt_pk_f16_f32 v125, v6, v7
	v_lshl_add_u64 v[8:9], v[168:169], 0, s[2:3]
	s_waitcnt vmcnt(14)
	v_pk_mul_f32 v[6:7], v[190:191], s[22:23] op_sel_hi:[1,0]
	s_nop 0
	v_cvt_pk_f16_f32 v162, v6, v7
	v_pk_mul_f32 v[6:7], v[192:193], s[22:23] op_sel_hi:[1,0]
	global_load_dwordx4 v[190:193], v[8:9], off offset:16
	global_load_dwordx4 v[238:241], v[8:9], off
	v_cvt_pk_f16_f32 v163, v6, v7
	v_pk_mul_f32 v[6:7], v[186:187], s[22:23] op_sel_hi:[1,0]
	v_lshl_add_u64 v[8:9], v[168:169], 0, s[18:19]
	v_cvt_pk_f16_f32 v164, v6, v7
	v_pk_mul_f32 v[6:7], v[188:189], s[22:23] op_sel_hi:[1,0]
	s_waitcnt vmcnt(4)
	v_pk_mul_f32 v[86:87], v[86:87], s[14:15] op_sel_hi:[1,0]
	v_cvt_pk_f16_f32 v165, v6, v7
	v_lshl_add_u64 v[6:7], v[166:167], 0, s[2:3]
	global_load_dwordx4 v[186:189], v[6:7], off offset:16
	global_load_dwordx4 v[242:245], v[6:7], off
	v_pk_mul_f32 v[6:7], v[146:147], s[22:23] op_sel_hi:[1,0]
	ds_write_b128 v214, v[162:165] offset:5120
	v_cvt_pk_f16_f32 v134, v6, v7
	v_pk_mul_f32 v[6:7], v[148:149], s[22:23] op_sel_hi:[1,0]
	s_waitcnt vmcnt(4)
	v_pk_mul_f32 v[82:83], v[82:83], s[14:15] op_sel_hi:[1,0]
	v_cvt_pk_f16_f32 v135, v6, v7
	v_lshl_add_u64 v[6:7], v[144:145], 0, s[18:19]
	global_load_dwordx4 v[246:249], v[6:7], off offset:16
	global_load_dwordx4 v[162:165], v[6:7], off
	global_load_dwordx4 v[250:253], v[8:9], off offset:16
	global_load_dwordx4 v[178:181], v[8:9], off
	v_pk_mul_f32 v[6:7], v[136:137], s[22:23] op_sel_hi:[1,0]
	v_pk_mul_f32 v[146:147], v[224:225], s[14:15] op_sel_hi:[1,0]
	v_cvt_pk_f16_f32 v136, v6, v7
	v_pk_mul_f32 v[6:7], v[138:139], s[22:23] op_sel_hi:[1,0]
	v_lshl_add_u64 v[138:139], v[144:145], 0, s[16:17]
	v_cvt_pk_f16_f32 v137, v6, v7
	v_pk_mul_f32 v[6:7], v[198:199], s[14:15] op_sel_hi:[1,0]
	v_pk_mul_f32 v[144:145], v[228:229], s[14:15] op_sel_hi:[1,0]
	v_cvt_pk_f16_f32 v198, v6, v7
	v_pk_mul_f32 v[6:7], v[200:201], s[14:15] op_sel_hi:[1,0]
	s_lshr_b32 s2, s15, 7
	v_cvt_pk_f16_f32 v199, v6, v7
	v_pk_mul_f32 v[6:7], v[194:195], s[14:15] op_sel_hi:[1,0]
	s_nop 0
	v_cvt_pk_f16_f32 v200, v6, v7
	v_pk_mul_f32 v[6:7], v[196:197], s[14:15] op_sel_hi:[1,0]
	s_nop 0
	v_cvt_pk_f16_f32 v201, v6, v7
	v_pk_mul_f32 v[6:7], v[150:151], s[14:15] op_sel_hi:[1,0]
	ds_write_b128 v214, v[198:201] offset:38912
	v_cvt_pk_f16_f32 v202, v6, v7
	v_pk_mul_f32 v[6:7], v[152:153], s[14:15] op_sel_hi:[1,0]
	v_cvt_pk_f16_f32 v150, v82, v83
	v_cvt_pk_f16_f32 v203, v6, v7
	v_lshl_add_u64 v[6:7], v[166:167], 0, s[18:19]
	global_load_dwordx4 v[194:197], v[6:7], off offset:16
	global_load_dwordx4 v[218:221], v[6:7], off
	v_pk_mul_f32 v[6:7], v[140:141], s[14:15] op_sel_hi:[1,0]
	v_pk_mul_f32 v[82:83], v[84:85], s[14:15] op_sel_hi:[1,0]
	v_cvt_pk_f16_f32 v204, v6, v7
	v_pk_mul_f32 v[6:7], v[142:143], s[14:15] op_sel_hi:[1,0]
	v_cvt_pk_f16_f32 v151, v82, v83
	v_cvt_pk_f16_f32 v205, v6, v7
	ds_write_b128 v214, v[202:205] offset:39936
	global_load_dwordx4 v[6:9], v[138:139], off offset:16
	global_load_dwordx4 v[230:233], v[138:139], off
	v_pk_mul_f32 v[82:83], v[170:171], s[14:15] op_sel_hi:[1,0]
	v_pk_mul_f32 v[138:139], v[158:159], s[14:15] op_sel_hi:[1,0]
	v_cvt_pk_f16_f32 v152, v82, v83
	v_pk_mul_f32 v[82:83], v[172:173], s[14:15] op_sel_hi:[1,0]
	v_pk_mul_f32 v[140:141], v[160:161], s[14:15] op_sel_hi:[1,0]
	v_cvt_pk_f16_f32 v153, v82, v83
	s_waitcnt vmcnt(10)
	v_pk_mul_f32 v[82:83], v[238:239], s[14:15] op_sel_hi:[1,0]
	v_cvt_pk_f16_f32 v138, v138, v139
	v_cvt_pk_f16_f32 v139, v140, v141
	v_pk_mul_f32 v[140:141], v[154:155], s[14:15] op_sel_hi:[1,0]
	v_cvt_pk_f16_f32 v154, v82, v83
	v_pk_mul_f32 v[82:83], v[240:241], s[14:15] op_sel_hi:[1,0]
	v_pk_mul_f32 v[142:143], v[156:157], s[14:15] op_sel_hi:[1,0]
	v_cvt_pk_f16_f32 v155, v82, v83
	v_pk_mul_f32 v[82:83], v[190:191], s[14:15] op_sel_hi:[1,0]
	v_cvt_pk_f16_f32 v140, v140, v141
	v_cvt_pk_f16_f32 v156, v82, v83
	v_pk_mul_f32 v[82:83], v[192:193], s[14:15] op_sel_hi:[1,0]
	v_cvt_pk_f16_f32 v141, v142, v143
	v_cvt_pk_f16_f32 v157, v82, v83
	v_pk_mul_f32 v[142:143], v[226:227], s[14:15] op_sel_hi:[1,0]
	v_lshl_add_u64 v[166:167], v[166:167], 0, s[16:17]
	v_cvt_pk_f16_f32 v142, v142, v143
	v_cvt_pk_f16_f32 v143, v144, v145
	v_pk_mul_f32 v[144:145], v[222:223], s[14:15] op_sel_hi:[1,0]
	v_and_b32_e32 v239, 3, v0
	v_cvt_pk_f16_f32 v144, v144, v145
	v_cvt_pk_f16_f32 v145, v146, v147
	v_cvt_pk_f16_f32 v146, v86, v87
	v_pk_mul_f32 v[86:87], v[88:89], s[14:15] op_sel_hi:[1,0]
	v_bfe_u32 v0, v0, 2, 3
	v_cvt_pk_f16_f32 v147, v86, v87
	v_pk_mul_f32 v[86:87], v[206:207], s[14:15] op_sel_hi:[1,0]
	v_cmp_eq_u32_e32 vcc, 0, v239
	v_cvt_pk_f16_f32 v148, v86, v87
	v_pk_mul_f32 v[86:87], v[208:209], s[14:15] op_sel_hi:[1,0]
	s_waitcnt vmcnt(8)
	v_pk_mul_f32 v[82:83], v[242:243], s[14:15] op_sel_hi:[1,0]
	v_cvt_pk_f16_f32 v149, v86, v87
	v_cvt_pk_f16_f32 v158, v82, v83
	v_pk_mul_f32 v[82:83], v[244:245], s[14:15] op_sel_hi:[1,0]
	v_lshl_add_u64 v[86:87], v[168:169], 0, s[16:17]
	v_cvt_pk_f16_f32 v159, v82, v83
	v_pk_mul_f32 v[82:83], v[186:187], s[14:15] op_sel_hi:[1,0]
	v_lshlrev_b32_e32 v245, 4, v255
	v_cvt_pk_f16_f32 v160, v82, v83
	v_pk_mul_f32 v[82:83], v[188:189], s[14:15] op_sel_hi:[1,0]
	s_waitcnt vmcnt(4)
	v_pk_mul_f32 v[170:171], v[178:179], s[14:15] op_sel_hi:[1,0]
	v_cvt_pk_f16_f32 v161, v82, v83
	v_pk_mul_f32 v[82:83], v[162:163], s[14:15] op_sel_hi:[1,0]
	v_cvt_pk_f16_f32 v168, v170, v171
	v_cvt_pk_f16_f32 v162, v82, v83
	v_pk_mul_f32 v[82:83], v[164:165], s[14:15] op_sel_hi:[1,0]
	v_pk_mul_f32 v[170:171], v[180:181], s[14:15] op_sel_hi:[1,0]
	v_cvt_pk_f16_f32 v163, v82, v83
	v_pk_mul_f32 v[82:83], v[246:247], s[14:15] op_sel_hi:[1,0]
	v_cvt_pk_f16_f32 v169, v170, v171
	v_cvt_pk_f16_f32 v164, v82, v83
	v_pk_mul_f32 v[82:83], v[248:249], s[14:15] op_sel_hi:[1,0]
	v_pk_mul_f32 v[170:171], v[250:251], s[14:15] op_sel_hi:[1,0]
	v_cvt_pk_f16_f32 v165, v82, v83
	global_load_dwordx4 v[82:85], v[86:87], off offset:16
	s_nop 0
	global_load_dwordx4 v[86:89], v[86:87], off
	s_nop 0
	global_load_dwordx4 v[186:189], v[166:167], off offset:16
	global_load_dwordx4 v[178:181], v[166:167], off
	v_pk_mul_f32 v[172:173], v[252:253], s[14:15] op_sel_hi:[1,0]
	v_cvt_pk_f16_f32 v170, v170, v171
	v_cvt_pk_f16_f32 v171, v172, v173
	ds_write_b128 v214, v[168:171] offset:6144
	v_or_b32_e32 v210, v245, v254
	s_waitcnt vmcnt(7)
	v_pk_mul_f32 v[170:171], v[196:197], s[14:15] op_sel_hi:[1,0]
	s_waitcnt vmcnt(6)
	v_pk_mul_f32 v[166:167], v[218:219], s[14:15] op_sel_hi:[1,0]
	v_pk_mul_f32 v[168:169], v[220:221], s[14:15] op_sel_hi:[1,0]
	v_cvt_pk_f16_f32 v166, v166, v167
	v_cvt_pk_f16_f32 v167, v168, v169
	v_pk_mul_f32 v[168:169], v[194:195], s[14:15] op_sel_hi:[1,0]
	v_add_u32_e32 v219, 0x8000, v214
	v_cvt_pk_f16_f32 v168, v168, v169
	v_cvt_pk_f16_f32 v169, v170, v171
	s_waitcnt vmcnt(4)
	v_pk_mul_f32 v[170:171], v[230:231], s[14:15] op_sel_hi:[1,0]
	v_pk_mul_f32 v[172:173], v[232:233], s[14:15] op_sel_hi:[1,0]
	v_pk_mul_f32 v[6:7], v[6:7], s[14:15] op_sel_hi:[1,0]
	v_cvt_pk_f16_f32 v170, v170, v171
	v_cvt_pk_f16_f32 v171, v172, v173
	v_cvt_pk_f16_f32 v172, v6, v7
	v_pk_mul_f32 v[6:7], v[8:9], s[14:15] op_sel_hi:[1,0]
	s_waitcnt vmcnt(3)
	v_pk_mul_f32 v[82:83], v[82:83], s[14:15] op_sel_hi:[1,0]
	v_cvt_pk_f16_f32 v173, v6, v7
	v_accvgpr_read_b32 v6, a34
	v_lshrrev_b32_e32 v238, 5, v6
	v_lshlrev_b32_e32 v6, 2, v238
	v_lshl_or_b32 v228, s2, 3, v6
	v_or_b32_e32 v240, v228, v239
	v_add_u32_e32 v6, v240, v216
	v_ashrrev_i32_e32 v7, 31, v6
	v_lshlrev_b64 v[8:9], 2, v[6:7]
	v_lshl_add_u64 v[190:191], s[8:9], 0, v[8:9]
	v_lshl_add_u64 v[192:193], s[10:11], 0, v[8:9]
	v_lshl_add_u64 v[194:195], s[4:5], 0, v[8:9]
	v_lshl_add_u64 v[8:9], s[6:7], 0, v[8:9]
	global_load_dword v220, v[190:191], off
	global_load_dword v222, v[190:191], off offset:2048
	global_load_dword v221, v[192:193], off
	global_load_dword v223, v[192:193], off offset:2048
	global_load_dword v224, v[194:195], off
	global_load_dword v225, v[194:195], off offset:2048
	global_load_dword v226, v[8:9], off
	global_load_dword v227, v[8:9], off offset:2048
	v_add_u32_e32 v8, 0x400, v6
	v_ashrrev_i32_e32 v9, 31, v8
	v_lshlrev_b64 v[8:9], 2, v[8:9]
	v_lshl_add_u64 v[190:191], s[8:9], 0, v[8:9]
	global_load_dword v229, v[190:191], off
	v_lshl_add_u64 v[190:191], s[10:11], 0, v[8:9]
	v_add_u32_e32 v6, 0x600, v6
	global_load_dword v241, v[190:191], off
	v_lshl_add_u64 v[190:191], s[4:5], 0, v[8:9]
	v_ashrrev_i32_e32 v7, 31, v6
	global_load_dword v242, v[190:191], off
	v_lshlrev_b64 v[190:191], 2, v[6:7]
	v_lshl_add_u64 v[6:7], s[8:9], 0, v[190:191]
	v_lshl_add_u64 v[8:9], s[6:7], 0, v[8:9]
	global_load_dword v244, v[6:7], off
	v_lshlrev_b64 v[6:7], 9, v[210:211]
	global_load_dword v243, v[8:9], off
	v_lshl_add_u64 v[6:7], s[12:13], 0, v[6:7]
	v_accvgpr_read_b32 v8, a33
	v_lshl_add_u64 v[6:7], s[0:1], 1, v[6:7]
	v_lshlrev_b32_e32 v210, 1, v8
	v_lshl_add_u64 v[212:213], v[6:7], 0, v[210:211]
	global_load_dwordx4 v[6:9], v[212:213], off
	s_waitcnt vmcnt(16)
	v_pk_mul_f32 v[86:87], v[86:87], s[14:15] op_sel_hi:[1,0]
	v_pk_mul_f32 v[88:89], v[88:89], s[14:15] op_sel_hi:[1,0]
	v_lshl_add_u64 v[192:193], s[10:11], 0, v[190:191]
	v_cvt_pk_f16_f32 v86, v86, v87
	v_cvt_pk_f16_f32 v87, v88, v89
	v_cvt_pk_f16_f32 v88, v82, v83
	v_pk_mul_f32 v[82:83], v[84:85], s[14:15] op_sel_hi:[1,0]
	global_load_dword v246, v[192:193], off
	v_lshl_add_u64 v[192:193], s[4:5], 0, v[190:191]
	v_lshl_add_u64 v[190:191], s[6:7], 0, v[190:191]
	v_cvt_pk_f16_f32 v89, v82, v83
	v_accvgpr_read_b32 v85, a32
	global_load_dwordx4 v[230:233], v[212:213], off offset:64
	global_load_dword v247, v[192:193], off
	global_load_dword v248, v[190:191], off
	ds_write_b128 v214, v[86:89] offset:7168
	v_lshlrev_b32_e32 v84, 14, v255
	v_lshlrev_b32_e32 v85, 8, v85
	v_lshlrev_b32_e32 v86, 4, v254
	s_lshl_b32 s4, s23, 12
	v_or3_b32 v85, v85, v86, v84
	s_lshl_b32 s0, s26, 10
	v_add_u32_e32 v85, s4, v85
	s_and_b32 s0, s0, 0xc00
	v_or_b32_e32 v216, s0, v85
	s_lshl_b32 s0, s27, 10
	s_waitcnt vmcnt(18)
	v_pk_mul_f32 v[82:83], v[178:179], s[14:15] op_sel_hi:[1,0]
	v_lshlrev_b32_e32 v86, 10, v215
	s_and_b32 s0, s0, 0xc00
	v_cvt_pk_f16_f32 v178, v82, v83
	v_pk_mul_f32 v[82:83], v[180:181], s[14:15] op_sel_hi:[1,0]
	v_and_b32_e32 v86, 0xc00, v86
	v_or_b32_e32 v217, s0, v85
	s_lshl_b32 s0, s30, 10
	v_cvt_pk_f16_f32 v179, v82, v83
	v_pk_mul_f32 v[82:83], v[186:187], s[14:15] op_sel_hi:[1,0]
	v_or_b32_e32 v210, v85, v86
	s_and_b32 s0, s0, 0xc00
	s_mov_b32 s30, 0x80000
	v_cvt_pk_f16_f32 v180, v82, v83
	v_pk_mul_f32 v[82:83], v[188:189], s[14:15] op_sel_hi:[1,0]
	v_or_b32_e32 v218, s0, v85
	buffer_load_dwordx4 v[186:189], v210, s[28:31], s31 offen sc1
	buffer_load_dwordx4 v[190:193], v216, s[28:31], s31 offen sc1
	buffer_load_dwordx4 v[194:197], v217, s[28:31], s31 offen sc1
	buffer_load_dwordx4 v[206:209], v218, s[28:31], s31 offen sc1
	v_cvt_pk_f16_f32 v181, v82, v83
	s_waitcnt vmcnt(8)
	v_mfma_f32_16x16x32_f16 a[0:3], a[0:3], v[6:9], 0
	v_add_f32_e32 v82, v220, v221
	v_mul_f32_e32 v220, 0x3fb8aa3b, v82
	v_add_f32_e32 v82, v224, v226
	v_mul_f32_e32 v221, 0x3fb8aa3b, v82
	v_add_f32_e32 v82, v222, v223
	v_mul_f32_e32 v222, 0x3fb8aa3b, v82
	v_add_f32_e32 v82, v225, v227
	v_mul_f32_e32 v223, 0x3fb8aa3b, v82
	v_add_f32_e32 v82, v229, v241
	v_mul_f32_e32 v224, 0x4038aa3b, v82
	v_add_f32_e32 v82, v242, v243
	s_lshr_b32 s0, s15, 3
	v_mul_f32_e32 v225, 0x4038aa3b, v82
	s_waitcnt vmcnt(7)
	v_add_f32_e32 v82, v244, v246
	v_mul_f32_e32 v226, 0x3fb8aa3b, v82
	s_waitcnt vmcnt(4)
	v_add_f32_e32 v82, v247, v248
	v_and_or_b32 v0, s0, 8, v0
	v_mfma_f32_16x16x32_f16 a[0:3], a[4:7], v[230:233], a[0:3]
	v_mul_f32_e32 v227, 0x3fb8aa3b, v82
	v_lshlrev_b32_e32 v82, 6, v228
	v_lshlrev_b32_e32 v83, 2, v239
	v_mfma_f32_16x16x32_f16 a[4:7], v[126:129], v[6:9], 0
	v_lshlrev_b32_e32 v85, 4, v0
	v_or3_b32 v82, v82, v85, v83
	v_add_u32_e32 v228, 0x14000, v82
	v_mfma_f32_16x16x32_f16 a[8:11], v[174:177], v[6:9], 0
	v_add_u32_e32 v229, 0x10000, v82
	v_lshlrev_b32_e32 v82, 9, v215
	s_lshl_b32 s0, s2, 8
	v_mfma_f32_16x16x32_f16 a[12:15], v[198:201], v[6:9], 0
	v_lshl_or_b32 v83, v238, 3, v84
	v_add_u32_e32 v6, s0, v82
	v_add_u32_e32 v6, v6, v83
	v_mfma_f32_16x16x32_f16 a[4:7], v[130:133], v[230:233], a[4:7]
	v_or_b32_e32 v6, v6, v85
	v_bfrev_b32_e32 v7, 1
	v_or_b32_e32 v0, v0, v245
	v_mfma_f32_16x16x32_f16 a[8:11], v[182:185], v[230:233], a[8:11]
	v_cndmask_b32_e32 v198, v7, v6, vcc
	v_lshlrev_b32_e32 v0, 11, v0
	v_mfma_f32_16x16x32_f16 a[12:15], v[202:205], v[230:233], a[12:15]
	v_lshlrev_b32_e32 v6, 6, v215
	v_lshlrev_b32_e32 v7, 2, v240
	s_add_i32 s2, s4, 0x10000
	s_add_i32 s4, s4, 0x14000
	s_brev_b32 s26, 8
	s_mov_b32 s27, s31
	v_add3_u32 v199, v7, v6, v0
	v_cmp_lt_u32_e64 s[0:1], 1, v239
	v_or_b32_e32 v200, s2, v1
	v_or_b32_e32 v201, s4, v1
	s_mov_b64 s[4:5], 0
	s_mov_b32 s6, 0
	v_mov_b32_e32 v0, v211
	s_waitcnt lgkmcnt(0)
	ds_read_b128 a[36:39], v219
	ds_read_b128 a[40:43], v219 offset:1024
	ds_read_b128 a[44:47], v219 offset:2048
	ds_read_b128 a[48:51], v219 offset:3072
	ds_read_b128 a[52:55], v219 offset:4096
	ds_read_b128 a[56:59], v219 offset:5120
	ds_read_b128 a[60:63], v219 offset:6144
	ds_read_b128 a[64:67], v219 offset:7168
	s_waitcnt lgkmcnt(0)
	ds_read_b128 a[68:71], v214
	ds_read_b128 a[72:75], v214 offset:1024
	ds_read_b128 a[76:79], v214 offset:2048
	ds_read_b128 a[80:83], v214 offset:3072
	ds_read_b128 a[84:87], v214 offset:4096
	ds_read_b128 a[88:91], v214 offset:5120
	ds_read_b128 a[92:95], v214 offset:6144
	ds_read_b128 a[96:99], v214 offset:7168
	s_waitcnt vmcnt(0) lgkmcnt(0)
	s_mov_b32 s4, 0
	s_mov_b32 s6, 0
	s_mov_b32 s3, 0
.Lfast_tick:
	s_add_i32 s7, s6, -1
	s_lshl_b32 s2, s7, 29
	s_andn2_b32 s8, 2.0, s2
	s_lshl_b32 s2, s7, 17
	s_and_b32 s10, s2, 0x20000
	s_or_b32 s14, s10, 0x40000
	s_lshl_b32 s2, s6, 17
	s_and_b32 s11, s2, 0x20000
	s_or_b32 s15, s11, 0x40000
	s_lshl_b32 s2, s6, 29
	s_andn2_b32 s9, 2.0, s2
	s_cmp_eq_u32 s6, 0
	s_cselect_b64 s[12:13], -1, 0
	s_waitcnt vmcnt(5)
	v_bitop3_b32 v1, v187, v189, s8 bitop3:0x7e
	v_and_b32_e32 v187, 0xbfffffff, v187
	v_and_b32_e32 v189, 0xbfffffff, v189
	s_nop 1
	v_mfma_f32_16x16x32_f16 a[16:19], v[2:5], v[186:189], a[0:3]
	v_mfma_f32_16x16x32_f16 a[20:23], v[42:45], v[186:189], a[4:7]
	v_mfma_f32_16x16x32_f16 a[24:27], v[90:93], v[186:189], a[8:11]
	v_mfma_f32_16x16x32_f16 a[28:31], v[138:141], v[186:189], a[12:15]
	s_add_i32 s2, s6, 1
	s_min_u32 s2, s2, 0x3ff
	s_lshl_b32 s2, s2, 16
	v_lshl_add_u64 v[238:239], v[212:213], 0, s[2:3]
	global_load_dwordx4 v[86:89], v[238:239], off
	s_waitcnt vmcnt(5)
	v_bitop3_b32 v202, v191, v193, s8 bitop3:0x7e
	v_and_b32_e32 v191, 0xbfffffff, v191
	v_and_b32_e32 v193, 0xbfffffff, v193
	s_nop 1
	v_mfma_f32_16x16x32_f16 a[16:19], v[14:17], v[190:193], a[16:19]
	v_mfma_f32_16x16x32_f16 a[20:23], v[54:57], v[190:193], a[20:23]
	v_mfma_f32_16x16x32_f16 a[24:27], v[102:105], v[190:193], a[24:27]
	v_mfma_f32_16x16x32_f16 a[28:31], v[150:153], v[190:193], a[28:31]
	global_load_dwordx4 v[82:85], v[238:239], off offset:64
	s_waitcnt vmcnt(5)
	v_bitop3_b32 v203, v195, v197, s8 bitop3:0x7e
	v_and_b32_e32 v195, 0xbfffffff, v195
	v_and_b32_e32 v197, 0xbfffffff, v197
	s_nop 1
	v_mfma_f32_16x16x32_f16 a[16:19], v[26:29], v[194:197], a[16:19]
	v_mfma_f32_16x16x32_f16 a[20:23], v[66:69], v[194:197], a[20:23]
	v_mfma_f32_16x16x32_f16 a[24:27], v[114:117], v[194:197], a[24:27]
	v_mfma_f32_16x16x32_f16 a[28:31], v[162:165], v[194:197], a[28:31]
	s_waitcnt vmcnt(4)
	v_bitop3_b32 v204, v207, v209, s8 bitop3:0x7e
	v_and_b32_e32 v207, 0xbfffffff, v207
	v_and_b32_e32 v209, 0xbfffffff, v209
	s_nop 1
	v_mfma_f32_16x16x32_f16 a[16:19], v[34:37], v[206:209], a[16:19]
	v_mfma_f32_16x16x32_f16 a[20:23], v[74:77], v[206:209], a[20:23]
	v_mfma_f32_16x16x32_f16 a[24:27], v[122:125], v[206:209], a[24:27]
	v_mfma_f32_16x16x32_f16 a[28:31], v[170:173], v[206:209], a[28:31]
	v_or3_b32 v1, v1, v202, v203
	v_bitop3_b32 v1, v1, 2.0, v204 bitop3:0xc8
	v_cmp_ne_u32_e32 vcc, 0, v1
	s_cmp_lg_u64 vcc, 0
	s_cbranch_scc1 .LredoA
.LcontA:
	s_nop 2
	ds_write_b128 v200, a[16:19]
	ds_write_b128 v200, a[20:23] offset:1024
	ds_write_b128 v200, a[24:27] offset:2048
	ds_write_b128 v200, a[28:31] offset:3072
	v_mfma_f32_16x16x32_f16 a[100:103], v[234:237], v[186:189], 0
	v_mfma_f32_16x16x32_f16 a[104:107], v[46:49], v[186:189], 0
	buffer_load_dwordx4 v[6:9], v210, s[28:31], s14 offen sc1
	v_mfma_f32_16x16x32_f16 a[108:111], v[94:97], v[186:189], 0
	v_mfma_f32_16x16x32_f16 a[112:115], v[142:145], v[186:189], 0
	buffer_load_dwordx4 v[130:133], v216, s[28:31], s14 offen sc1
	v_mfma_f32_16x16x32_f16 a[100:103], v[18:21], v[190:193], a[100:103]
	v_mfma_f32_16x16x32_f16 a[104:107], v[58:61], v[190:193], a[104:107]
	s_waitcnt lgkmcnt(0)
	s_barrier
	ds_read2st64_b32 v[240:241], v229 offset1:8
	ds_read2st64_b32 v[242:243], v229 offset0:16 offset1:24
	ds_read2st64_b32 v[244:245], v229 offset0:32 offset1:40
	ds_read2st64_b32 v[246:247], v229 offset0:48 offset1:56
	ds_read2st64_b32 v[248:249], v229 offset0:4 offset1:12
	ds_read2st64_b32 v[250:251], v229 offset0:20 offset1:28
	ds_read2st64_b32 v[252:253], v229 offset0:36 offset1:44
	ds_read2st64_b32 v[254:255], v229 offset0:52 offset1:60
	s_waitcnt lgkmcnt(7)
	v_sub_f32_e32 v126, v240, v220
	v_add_f32_e32 v127, v224, v241
	v_mfma_f32_16x16x32_f16 a[108:111], v[106:109], v[190:193], a[108:111]
	s_waitcnt lgkmcnt(6)
	v_add_f32_e32 v126, v126, v242
	v_add_f32_e32 v127, v127, v243
	s_waitcnt lgkmcnt(5)
	v_add_f32_e32 v126, v126, v244
	v_mfma_f32_16x16x32_f16 a[112:115], v[154:157], v[190:193], a[112:115]
	v_add_f32_e32 v127, v127, v245
	s_waitcnt lgkmcnt(4)
	v_add_f32_e32 v126, v126, v246
	v_add_f32_e32 v127, v127, v247
	buffer_load_dwordx4 v[174:177], v217, s[28:31], s14 offen sc1
	v_exp_f32_e32 v127, v127
	v_exp_f32_e32 v126, v126
	s_waitcnt lgkmcnt(3)
	v_sub_f32_e32 v128, v248, v222
	v_mfma_f32_16x16x32_f16 a[100:103], a[68:71], v[194:197], a[100:103]
	v_sub_f32_e32 v129, v249, v226
	s_waitcnt lgkmcnt(2)
	v_add_f32_e32 v128, v128, v250
	v_add_f32_e32 v129, v129, v251
	v_mfma_f32_16x16x32_f16 a[104:107], a[76:79], v[194:197], a[104:107]
	s_waitcnt lgkmcnt(1)
	v_add_f32_e32 v128, v128, v252
	v_add_f32_e32 v129, v129, v253
	s_waitcnt lgkmcnt(0)
	v_add_f32_e32 v128, v128, v254
	buffer_load_dwordx4 v[182:185], v218, s[28:31], s14 offen sc1
	v_add_f32_e32 v129, v129, v255
	v_add_f32_e32 v127, 1.0, v127
	v_add_f32_e32 v126, 1.0, v126
	v_mfma_f32_16x16x32_f16 a[108:111], a[84:87], v[194:197], a[108:111]
	v_exp_f32_e32 v128, v128
	v_exp_f32_e32 v129, v129
	v_rcp_f32_e32 v127, v127
	v_mfma_f32_16x16x32_f16 a[112:115], a[92:95], v[194:197], a[112:115]
	v_rcp_f32_e32 v126, v126
	v_add_f32_e32 v128, 1.0, v128
	v_add_f32_e32 v129, 1.0, v129
	v_mfma_f32_16x16x32_f16 a[100:103], a[72:75], v[206:209], a[100:103]
	v_fma_f32 v127, v127, -2.0, 1.0
	v_rcp_f32_e32 v128, v128
	v_mul_f32_e32 v126, v126, v127
	v_mfma_f32_16x16x32_f16 a[104:107], a[80:83], v[206:209], a[104:107]
	v_rcp_f32_e32 v129, v129
	s_nop 0
	v_fma_f32 v211, v128, v211, v126
	v_mfma_f32_16x16x32_f16 a[108:111], a[88:91], v[206:209], a[108:111]
	v_mul_f32_e32 v202, 0x4038aa3b, v211
	v_exp_f32_e32 v202, v202
	v_mov_b32_e32 v203, s9
	v_mfma_f32_16x16x32_f16 a[112:115], a[96:99], v[206:209], a[112:115]
	v_cndmask_b32_e64 v203, 0, v203, s[0:1]
	v_add_f32_e32 v202, 1.0, v202
	v_rcp_f32_e32 v202, v202
	s_nop 0
	v_fma_f32 v202, v202, -2.0, 1.0
	v_fma_mixlo_f16 v202, v129, v202, 0
	v_and_b32_e32 v1, 0xffff, v202
	s_nop 1
	v_mov_b32_dpp v204, v1 quad_perm:[1,0,3,2] row_mask:0xf bank_mask:0xf bound_ctrl:1
	v_lshlrev_b32_e32 v204, 16, v204
	v_and_b32_e32 v204, 0xbfff0000, v204
	v_or3_b32 v204, v204, v203, v1
	s_nop 1
	v_mov_b32_dpp v205, v204 quad_perm:[2,3,0,1] row_mask:0xf bank_mask:0xf bound_ctrl:1
	buffer_store_dwordx2 v[204:205], v198, s[28:31], s11 offen
	s_waitcnt vmcnt(4)
	v_bitop3_b32 v1, v7, v9, s8 bitop3:0x7e
	v_and_b32_e32 v7, 0xbfffffff, v7
	v_and_b32_e32 v9, 0xbfffffff, v9
	s_nop 1
	v_mfma_f32_16x16x32_f16 a[116:119], v[10:13], v[6:9], a[100:103]
	v_mfma_f32_16x16x32_f16 a[120:123], v[50:53], v[6:9], a[104:107]
	v_mfma_f32_16x16x32_f16 a[124:127], v[98:101], v[6:9], a[108:111]
	v_mfma_f32_16x16x32_f16 a[128:131], v[146:149], v[6:9], a[112:115]
	s_waitcnt vmcnt(3)
	v_bitop3_b32 v202, v131, v133, s8 bitop3:0x7e
	v_and_b32_e32 v131, 0xbfffffff, v131
	v_and_b32_e32 v133, 0xbfffffff, v133
	s_nop 1
	v_mfma_f32_16x16x32_f16 a[116:119], v[22:25], v[130:133], a[116:119]
	v_mfma_f32_16x16x32_f16 a[120:123], v[62:65], v[130:133], a[120:123]
	v_mfma_f32_16x16x32_f16 a[124:127], v[110:113], v[130:133], a[124:127]
	v_mfma_f32_16x16x32_f16 a[128:131], v[158:161], v[130:133], a[128:131]
	s_waitcnt vmcnt(2)
	v_bitop3_b32 v203, v175, v177, s8 bitop3:0x7e
	v_and_b32_e32 v175, 0xbfffffff, v175
	v_and_b32_e32 v177, 0xbfffffff, v177
	s_nop 1
	v_mfma_f32_16x16x32_f16 a[116:119], v[30:33], v[174:177], a[116:119]
	v_mfma_f32_16x16x32_f16 a[120:123], v[70:73], v[174:177], a[120:123]
	v_mfma_f32_16x16x32_f16 a[124:127], v[118:121], v[174:177], a[124:127]
	v_mfma_f32_16x16x32_f16 a[128:131], v[166:169], v[174:177], a[128:131]
	s_waitcnt vmcnt(1)
	v_bitop3_b32 v204, v183, v185, s8 bitop3:0x7e
	v_and_b32_e32 v183, 0xbfffffff, v183
	v_and_b32_e32 v185, 0xbfffffff, v185
	s_nop 1
	v_mfma_f32_16x16x32_f16 a[116:119], v[38:41], v[182:185], a[116:119]
	v_mfma_f32_16x16x32_f16 a[120:123], v[78:81], v[182:185], a[120:123]
	v_mfma_f32_16x16x32_f16 a[124:127], v[134:137], v[182:185], a[124:127]
	v_mfma_f32_16x16x32_f16 a[128:131], v[178:181], v[182:185], a[128:131]
	v_or3_b32 v1, v1, v202, v203
	v_bitop3_b32 v1, v1, 2.0, v204 bitop3:0xc8
	v_cmp_ne_u32_e32 vcc, 0, v1
	s_cmp_lg_u64 vcc, 0
	s_cbranch_scc1 .LredoB
.LcontB:
	s_nop 2
	ds_write_b128 v201, a[116:119]
	ds_write_b128 v201, a[120:123] offset:1024
	ds_write_b128 v201, a[124:127] offset:2048
	ds_write_b128 v201, a[128:131] offset:3072
	v_mfma_f32_16x16x32_f16 a[0:3], a[36:39], v[86:89], 0
	v_mfma_f32_16x16x32_f16 a[4:7], a[44:47], v[86:89], 0
	buffer_load_dwordx4 v[186:189], v210, s[28:31], s11 offen sc1
	v_mfma_f32_16x16x32_f16 a[8:11], a[52:55], v[86:89], 0
	v_mfma_f32_16x16x32_f16 a[12:15], a[60:63], v[86:89], 0
	buffer_load_dwordx4 v[190:193], v216, s[28:31], s11 offen sc1
	s_waitcnt lgkmcnt(0)
	s_barrier
	ds_read2st64_b32 v[240:241], v228 offset1:8
	ds_read2st64_b32 v[242:243], v228 offset0:16 offset1:24
	ds_read2st64_b32 v[244:245], v228 offset0:32 offset1:40
	ds_read2st64_b32 v[246:247], v228 offset0:48 offset1:56
	ds_read2st64_b32 v[248:249], v228 offset0:4 offset1:12
	ds_read2st64_b32 v[250:251], v228 offset0:20 offset1:28
	ds_read2st64_b32 v[252:253], v228 offset0:36 offset1:44
	ds_read2st64_b32 v[254:255], v228 offset0:52 offset1:60
	s_waitcnt lgkmcnt(7)
	v_sub_f32_e32 v126, v240, v221
	v_add_f32_e32 v127, v225, v241
	v_mfma_f32_16x16x32_f16 a[0:3], a[40:43], v[82:85], a[0:3]
	s_waitcnt lgkmcnt(6)
	v_add_f32_e32 v126, v126, v242
	v_add_f32_e32 v127, v127, v243
	s_waitcnt lgkmcnt(5)
	v_add_f32_e32 v126, v126, v244
	v_add_f32_e32 v127, v127, v245
	buffer_load_dwordx4 v[194:197], v217, s[28:31], s11 offen sc1
	s_waitcnt lgkmcnt(4)
	v_add_f32_e32 v126, v126, v246
	v_add_f32_e32 v127, v127, v247
	v_exp_f32_e32 v127, v127
	v_exp_f32_e32 v126, v126
	v_mfma_f32_16x16x32_f16 a[4:7], a[48:51], v[82:85], a[4:7]
	s_waitcnt lgkmcnt(3)
	v_sub_f32_e32 v128, v248, v223
	v_sub_f32_e32 v129, v249, v227
	s_waitcnt lgkmcnt(2)
	v_add_f32_e32 v128, v128, v250
	v_add_f32_e32 v129, v129, v251
	buffer_load_dwordx4 v[206:209], v218, s[28:31], s11 offen sc1
	s_waitcnt lgkmcnt(1)
	v_add_f32_e32 v128, v128, v252
	v_add_f32_e32 v129, v129, v253
	s_waitcnt lgkmcnt(0)
	v_add_f32_e32 v128, v128, v254
	v_add_f32_e32 v129, v129, v255
	v_mfma_f32_16x16x32_f16 a[8:11], a[56:59], v[82:85], a[8:11]
	v_add_f32_e32 v127, 1.0, v127
	v_add_f32_e32 v126, 1.0, v126
	v_exp_f32_e32 v128, v128
	v_exp_f32_e32 v129, v129
	v_mfma_f32_16x16x32_f16 a[12:15], a[64:67], v[82:85], a[12:15]
	v_rcp_f32_e32 v127, v127
	v_rcp_f32_e32 v126, v126
	v_add_f32_e32 v128, 1.0, v128
	v_add_f32_e32 v129, 1.0, v129
	v_fma_f32 v127, v127, -2.0, 1.0
	v_rcp_f32_e32 v128, v128
	v_mul_f32_e32 v126, v126, v127
	v_rcp_f32_e32 v129, v129
	s_nop 0
	v_fma_f32 v0, v128, v0, v126
	v_mul_f32_e32 v202, 0x4038aa3b, v0
	v_exp_f32_e32 v202, v202
	v_mov_b32_e32 v203, s9
	v_cndmask_b32_e64 v203, 0, v203, s[0:1]
	v_add_f32_e32 v202, 1.0, v202
	v_rcp_f32_e32 v202, v202
	s_nop 0
	v_fma_f32 v202, v202, -2.0, 1.0
	v_mul_f32_e32 v202, v129, v202
	v_cndmask_b32_e64 v202, v202, 0, s[12:13]
	v_cvt_f16_f32_e32 v1, v202
	s_nop 1
	v_mov_b32_dpp v204, v1 quad_perm:[1,0,3,2] row_mask:0xf bank_mask:0xf bound_ctrl:1
	v_lshlrev_b32_e32 v204, 16, v204
	v_and_b32_e32 v204, 0xbfff0000, v204
	v_or3_b32 v204, v204, v203, v1
	s_nop 1
	v_mov_b32_dpp v205, v204 quad_perm:[2,3,0,1] row_mask:0xf bank_mask:0xf bound_ctrl:1
	buffer_store_dwordx2 v[204:205], v198, s[28:31], s15 offen
	v_lshl_add_u32 v1, s7, 18, v199
	v_cndmask_b32_e64 v1, v1, -16, s[12:13]
	buffer_store_dword v202, v1, s[24:27], 0 offen nt
	v_cndmask_b32_e64 v0, v0, 0, s[12:13]
	s_add_i32 s6, s6, 1
	s_cmpk_lg_i32 s6, 0x401
	s_cbranch_scc1 .Lfast_tick
	s_branch .LBB1_31
.LredoA:
	s_cmp_lg_u32 s4, 0
	s_cbranch_scc1 .LcontA
	s_mov_b32 s5, 0
.LredoA_loop:
	buffer_load_dwordx4 v[186:189], v210, s[28:31], s10 offen sc1
	buffer_load_dwordx4 v[190:193], v216, s[28:31], s10 offen sc1
	buffer_load_dwordx4 v[194:197], v217, s[28:31], s10 offen sc1
	buffer_load_dwordx4 v[206:209], v218, s[28:31], s10 offen sc1
	s_waitcnt vmcnt(0)
	v_bitop3_b32 v1, v187, v189, s8 bitop3:0x7e
	v_bitop3_b32 v202, v191, v193, s8 bitop3:0x7e
	v_bitop3_b32 v203, v195, v197, s8 bitop3:0x7e
	v_bitop3_b32 v204, v207, v209, s8 bitop3:0x7e
	v_or3_b32 v1, v1, v202, v203
	v_bitop3_b32 v1, v1, 2.0, v204 bitop3:0xc8
	v_cmp_ne_u32_e32 vcc, 0, v1
	s_cmp_eq_u64 vcc, 0
	s_cbranch_scc1 .LredoA_ok
	s_add_i32 s5, s5, 1
	s_cmp_lt_u32 s5, 0x100000
	s_cbranch_scc1 .LredoA_loop
	s_mov_b32 s4, 1
.LredoA_ok:
	v_and_b32_e32 v187, 0xbfffffff, v187
	v_and_b32_e32 v189, 0xbfffffff, v189
	v_and_b32_e32 v191, 0xbfffffff, v191
	v_and_b32_e32 v193, 0xbfffffff, v193
	v_and_b32_e32 v195, 0xbfffffff, v195
	v_and_b32_e32 v197, 0xbfffffff, v197
	v_and_b32_e32 v207, 0xbfffffff, v207
	v_and_b32_e32 v209, 0xbfffffff, v209
	s_nop 1
	v_mfma_f32_16x16x32_f16 a[16:19], v[2:5], v[186:189], a[0:3]
	v_mfma_f32_16x16x32_f16 a[20:23], v[42:45], v[186:189], a[4:7]
	v_mfma_f32_16x16x32_f16 a[24:27], v[90:93], v[186:189], a[8:11]
	v_mfma_f32_16x16x32_f16 a[28:31], v[138:141], v[186:189], a[12:15]
	v_mfma_f32_16x16x32_f16 a[16:19], v[14:17], v[190:193], a[16:19]
	v_mfma_f32_16x16x32_f16 a[20:23], v[54:57], v[190:193], a[20:23]
	v_mfma_f32_16x16x32_f16 a[24:27], v[102:105], v[190:193], a[24:27]
	v_mfma_f32_16x16x32_f16 a[28:31], v[150:153], v[190:193], a[28:31]
	v_mfma_f32_16x16x32_f16 a[16:19], v[26:29], v[194:197], a[16:19]
	v_mfma_f32_16x16x32_f16 a[20:23], v[66:69], v[194:197], a[20:23]
	v_mfma_f32_16x16x32_f16 a[24:27], v[114:117], v[194:197], a[24:27]
	v_mfma_f32_16x16x32_f16 a[28:31], v[162:165], v[194:197], a[28:31]
	v_mfma_f32_16x16x32_f16 a[16:19], v[34:37], v[206:209], a[16:19]
	v_mfma_f32_16x16x32_f16 a[20:23], v[74:77], v[206:209], a[20:23]
	v_mfma_f32_16x16x32_f16 a[24:27], v[122:125], v[206:209], a[24:27]
	v_mfma_f32_16x16x32_f16 a[28:31], v[170:173], v[206:209], a[28:31]
	s_nop 4
	s_branch .LcontA

.LredoB_loop:
	buffer_load_dwordx4 v[6:9], v210, s[28:31], s14 offen sc1
	buffer_load_dwordx4 v[130:133], v216, s[28:31], s14 offen sc1
	buffer_load_dwordx4 v[174:177], v217, s[28:31], s14 offen sc1
	buffer_load_dwordx4 v[182:185], v218, s[28:31], s14 offen sc1
	s_waitcnt vmcnt(0)
	v_bitop3_b32 v1, v7, v9, s8 bitop3:0x7e
	v_bitop3_b32 v202, v131, v133, s8 bitop3:0x7e
	v_bitop3_b32 v203, v175, v177, s8 bitop3:0x7e
	v_bitop3_b32 v204, v183, v185, s8 bitop3:0x7e
	v_or3_b32 v1, v1, v202, v203
	v_bitop3_b32 v1, v1, 2.0, v204 bitop3:0xc8
	v_cmp_ne_u32_e32 vcc, 0, v1
	s_cmp_eq_u64 vcc, 0
	s_cbranch_scc1 .LredoB_ok
	s_add_i32 s5, s5, 1
	s_cmp_lt_u32 s5, 0x100000
	s_cbranch_scc1 .LredoB_loop
	s_mov_b32 s4, 1
.LredoB_ok:
	v_and_b32_e32 v7, 0xbfffffff, v7
	v_and_b32_e32 v9, 0xbfffffff, v9
	v_and_b32_e32 v131, 0xbfffffff, v131
	v_and_b32_e32 v133, 0xbfffffff, v133
	v_and_b32_e32 v175, 0xbfffffff, v175
	v_and_b32_e32 v177, 0xbfffffff, v177
	v_and_b32_e32 v183, 0xbfffffff, v183
	v_and_b32_e32 v185, 0xbfffffff, v185
	s_nop 1
	v_mfma_f32_16x16x32_f16 a[116:119], v[10:13], v[6:9], a[100:103]
	v_mfma_f32_16x16x32_f16 a[120:123], v[50:53], v[6:9], a[104:107]
	v_mfma_f32_16x16x32_f16 a[124:127], v[98:101], v[6:9], a[108:111]
	v_mfma_f32_16x16x32_f16 a[128:131], v[146:149], v[6:9], a[112:115]
	v_mfma_f32_16x16x32_f16 a[116:119], v[22:25], v[130:133], a[116:119]
	v_mfma_f32_16x16x32_f16 a[120:123], v[62:65], v[130:133], a[120:123]
	v_mfma_f32_16x16x32_f16 a[124:127], v[110:113], v[130:133], a[124:127]
	v_mfma_f32_16x16x32_f16 a[128:131], v[158:161], v[130:133], a[128:131]
	v_mfma_f32_16x16x32_f16 a[116:119], v[30:33], v[174:177], a[116:119]
	v_mfma_f32_16x16x32_f16 a[120:123], v[70:73], v[174:177], a[120:123]
	v_mfma_f32_16x16x32_f16 a[124:127], v[118:121], v[174:177], a[124:127]
	v_mfma_f32_16x16x32_f16 a[128:131], v[166:169], v[174:177], a[128:131]
	v_mfma_f32_16x16x32_f16 a[116:119], v[38:41], v[182:185], a[116:119]
	v_mfma_f32_16x16x32_f16 a[120:123], v[78:81], v[182:185], a[120:123]
	v_mfma_f32_16x16x32_f16 a[124:127], v[134:137], v[182:185], a[124:127]
	v_mfma_f32_16x16x32_f16 a[128:131], v[178:181], v[182:185], a[128:131]
	s_nop 4
	s_branch .LcontB

	.amdhsa_kernel _Z15lstm_persistentPKDF16_PKfS2_S2_S2_S2_S2_S2_S2_PfPjS4_
		.amdhsa_group_segment_fixed_size 98320
		.amdhsa_private_segment_fixed_size 0
		.amdhsa_kernarg_size 96
		.amdhsa_user_sgpr_count 2
		.amdhsa_user_sgpr_dispatch_ptr 0
		.amdhsa_user_sgpr_queue_ptr 0
		.amdhsa_user_sgpr_kernarg_segment_ptr 1
		.amdhsa_user_sgpr_dispatch_id 0
		.amdhsa_user_sgpr_kernarg_preload_length 0
		.amdhsa_user_sgpr_kernarg_preload_offset 0
		.amdhsa_user_sgpr_private_segment_size 0
		.amdhsa_uses_dynamic_stack 0
		.amdhsa_enable_private_segment 0
		.amdhsa_system_sgpr_workgroup_id_x 1
		.amdhsa_system_sgpr_workgroup_id_y 0
		.amdhsa_system_sgpr_workgroup_id_z 0
		.amdhsa_system_sgpr_workgroup_info 0
		.amdhsa_system_vgpr_workitem_id 0
		.amdhsa_next_free_vgpr 420
		.amdhsa_next_free_sgpr 96
		.amdhsa_accum_offset 256
		.amdhsa_reserve_vcc 1
		.amdhsa_float_round_mode_32 0
		.amdhsa_float_round_mode_16_64 0
		.amdhsa_float_denorm_mode_32 3
		.amdhsa_float_denorm_mode_16_64 3
		.amdhsa_dx10_clamp 1
		.amdhsa_ieee_mode 1
		.amdhsa_fp16_overflow 0
		.amdhsa_tg_split 0
		.amdhsa_exception_fp_ieee_invalid_op 0
		.amdhsa_exception_fp_denorm_src 0
		.amdhsa_exception_fp_ieee_div_zero 0
		.amdhsa_exception_fp_ieee_overflow 0
		.amdhsa_exception_fp_ieee_underflow 0
		.amdhsa_exception_fp_ieee_inexact 0
		.amdhsa_exception_int_div_zero 0
	.end_amdhsa_kernel

amdhsa.kernels:
  - .agpr_count:     0
    .args:
      - .actual_access:  read_only
        .address_space:  global
        .offset:         0
        .size:           8
        .value_kind:     global_buffer
      - .actual_access:  write_only
        .address_space:  global
        .offset:         8
        .size:           8
        .value_kind:     global_buffer
      - .offset:         16
        .size:           4
        .value_kind:     by_value
    .group_segment_fixed_size: 0
    .kernarg_segment_align: 8
    .kernarg_segment_size: 20
    .language:       OpenCL C
    .language_version:
      - 2
      - 0
    .max_flat_workgroup_size: 256
    .name:           _Z9x_to_halfPKfPDv8_DF16_i
    .private_segment_fixed_size: 0
    .sgpr_count:     10
    .sgpr_spill_count: 0
    .symbol:         _Z9x_to_halfPKfPDv8_DF16_i.kd
    .uniform_work_group_size: 1
    .uses_dynamic_stack: false
    .vgpr_count:     12
    .vgpr_spill_count: 0
    .wavefront_size: 64
  - .agpr_count:     164
    .args:
      - .actual_access:  read_only
        .address_space:  global
        .offset:         0
        .size:           8
        .value_kind:     global_buffer
      - .actual_access:  read_only
        .address_space:  global
        .offset:         8
        .size:           8
        .value_kind:     global_buffer
      - .actual_access:  read_only
        .address_space:  global
        .offset:         16
        .size:           8
        .value_kind:     global_buffer
      - .actual_access:  read_only
        .address_space:  global
        .offset:         24
        .size:           8
        .value_kind:     global_buffer
      - .actual_access:  read_only
        .address_space:  global
        .offset:         32
        .size:           8
        .value_kind:     global_buffer
      - .actual_access:  read_only
        .address_space:  global
        .offset:         40
        .size:           8
        .value_kind:     global_buffer
      - .actual_access:  read_only
        .address_space:  global
        .offset:         48
        .size:           8
        .value_kind:     global_buffer
      - .actual_access:  read_only
        .address_space:  global
        .offset:         56
        .size:           8
        .value_kind:     global_buffer
      - .actual_access:  read_only
        .address_space:  global
        .offset:         64
        .size:           8
        .value_kind:     global_buffer
      - .actual_access:  write_only
        .address_space:  global
        .offset:         72
        .size:           8
        .value_kind:     global_buffer
      - .address_space:  global
        .offset:         80
        .size:           8
        .value_kind:     global_buffer
      - .address_space:  global
        .offset:         88
        .size:           8
        .value_kind:     global_buffer
    .group_segment_fixed_size: 98320
    .kernarg_segment_align: 8
    .kernarg_segment_size: 96
    .language:       OpenCL C
    .language_version:
      - 2
      - 0
    .max_flat_workgroup_size: 256
    .name:           _Z15lstm_persistentPKDF16_PKfS2_S2_S2_S2_S2_S2_S2_PfPjS4_
    .private_segment_fixed_size: 0
    .sgpr_count:     50
    .sgpr_spill_count: 0
    .symbol:         _Z15lstm_persistentPKDF16_PKfS2_S2_S2_S2_S2_S2_S2_PfPjS4_.kd
    .uniform_work_group_size: 1
    .uses_dynamic_stack: false
    .vgpr_count:     420
    .vgpr_spill_count: 0
    .wavefront_size: 64
